# P2 FoX norm-bound task rewritten: coalesced rows (8 lanes per row), 32 loads in flight, DPP row sums
# speedup vs baseline: 1.0085x; 1.0044x over previous
.LBB0_387:
	s_ashr_i32 s6, s14, 7
	s_ashr_i32 s7, s6, 31
	s_lshl_b64 s[6:7], s[6:7], 25
	s_add_u32 s6, s8, s6
	s_addc_u32 s7, s9, s7
	s_and_b32 s15, s12, 0xf00000
	s_lshl_b32 s15, s15, 1
	s_add_u32 s6, s6, s15
	s_addc_u32 s7, s7, 0
	s_and_b32 s15, s10, 0x1c0
	s_lshl_b32 s15, s15, 1
	s_add_u32 s6, s6, s15
	s_addc_u32 s7, s7, 0
	v_lshrrev_b32_e32 v100, 3, v0
	v_and_b32_e32 v101, 7, v0
	v_lshlrev_b32_e32 v100, 10, v100
	v_lshl_or_b32 v100, v101, 4, v100
	s_mov_b64 s[98:99], s[6:7]
	global_load_dwordx4 v[104:107], v100, s[98:99]
	s_add_u32 s98, s98, 0x10000
	s_addc_u32 s99, s99, 0
	global_load_dwordx4 v[108:111], v100, s[98:99]
	s_add_u32 s98, s98, 0x10000
	s_addc_u32 s99, s99, 0
	global_load_dwordx4 v[112:115], v100, s[98:99]
	s_add_u32 s98, s98, 0x10000
	s_addc_u32 s99, s99, 0
	global_load_dwordx4 v[116:119], v100, s[98:99]
	s_add_u32 s98, s98, 0x10000
	s_addc_u32 s99, s99, 0
	global_load_dwordx4 v[120:123], v100, s[98:99]
	s_add_u32 s98, s98, 0x10000
	s_addc_u32 s99, s99, 0
	global_load_dwordx4 v[124:127], v100, s[98:99]
	s_add_u32 s98, s98, 0x10000
	s_addc_u32 s99, s99, 0
	global_load_dwordx4 v[128:131], v100, s[98:99]
	s_add_u32 s98, s98, 0x10000
	s_addc_u32 s99, s99, 0
	global_load_dwordx4 v[132:135], v100, s[98:99]
	s_add_u32 s98, s98, 0x10000
	s_addc_u32 s99, s99, 0
	global_load_dwordx4 v[136:139], v100, s[98:99]
	s_add_u32 s98, s98, 0x10000
	s_addc_u32 s99, s99, 0
	global_load_dwordx4 v[140:143], v100, s[98:99]
	s_add_u32 s98, s98, 0x10000
	s_addc_u32 s99, s99, 0
	global_load_dwordx4 v[144:147], v100, s[98:99]
	s_add_u32 s98, s98, 0x10000
	s_addc_u32 s99, s99, 0
	global_load_dwordx4 v[148:151], v100, s[98:99]
	s_add_u32 s98, s98, 0x10000
	s_addc_u32 s99, s99, 0
	global_load_dwordx4 v[152:155], v100, s[98:99]
	s_add_u32 s98, s98, 0x10000
	s_addc_u32 s99, s99, 0
	global_load_dwordx4 v[156:159], v100, s[98:99]
	s_add_u32 s98, s98, 0x10000
	s_addc_u32 s99, s99, 0
	global_load_dwordx4 v[160:163], v100, s[98:99]
	s_add_u32 s98, s98, 0x10000
	s_addc_u32 s99, s99, 0
	global_load_dwordx4 v[164:167], v100, s[98:99]
	s_add_u32 s98, s98, 0x10000
	s_addc_u32 s99, s99, 0
	global_load_dwordx4 v[168:171], v100, s[98:99]
	s_add_u32 s98, s98, 0x10000
	s_addc_u32 s99, s99, 0
	global_load_dwordx4 v[172:175], v100, s[98:99]
	s_add_u32 s98, s98, 0x10000
	s_addc_u32 s99, s99, 0
	global_load_dwordx4 v[176:179], v100, s[98:99]
	s_add_u32 s98, s98, 0x10000
	s_addc_u32 s99, s99, 0
	global_load_dwordx4 v[180:183], v100, s[98:99]
	s_add_u32 s98, s98, 0x10000
	s_addc_u32 s99, s99, 0
	global_load_dwordx4 v[184:187], v100, s[98:99]
	s_add_u32 s98, s98, 0x10000
	s_addc_u32 s99, s99, 0
	global_load_dwordx4 v[188:191], v100, s[98:99]
	s_add_u32 s98, s98, 0x10000
	s_addc_u32 s99, s99, 0
	global_load_dwordx4 v[192:195], v100, s[98:99]
	s_add_u32 s98, s98, 0x10000
	s_addc_u32 s99, s99, 0
	global_load_dwordx4 v[196:199], v100, s[98:99]
	s_add_u32 s98, s98, 0x10000
	s_addc_u32 s99, s99, 0
	global_load_dwordx4 v[200:203], v100, s[98:99]
	s_add_u32 s98, s98, 0x10000
	s_addc_u32 s99, s99, 0
	global_load_dwordx4 v[204:207], v100, s[98:99]
	s_add_u32 s98, s98, 0x10000
	s_addc_u32 s99, s99, 0
	global_load_dwordx4 v[208:211], v100, s[98:99]
	s_add_u32 s98, s98, 0x10000
	s_addc_u32 s99, s99, 0
	global_load_dwordx4 v[212:215], v100, s[98:99]
	s_add_u32 s98, s98, 0x10000
	s_addc_u32 s99, s99, 0
	global_load_dwordx4 v[216:219], v100, s[98:99]
	s_add_u32 s98, s98, 0x10000
	s_addc_u32 s99, s99, 0
	global_load_dwordx4 v[220:223], v100, s[98:99]
	s_add_u32 s98, s98, 0x10000
	s_addc_u32 s99, s99, 0
	global_load_dwordx4 v[224:227], v100, s[98:99]
	s_add_u32 s98, s98, 0x10000
	s_addc_u32 s99, s99, 0
	global_load_dwordx4 v[228:231], v100, s[98:99]
	s_mov_b32 s100, 0xffff0000
	v_mov_b32_e32 v2, 0
	s_waitcnt vmcnt(31)
	v_and_b32_e32 v101, s100, v104
	v_lshlrev_b32_e32 v104, 16, v104
	v_mul_f32_e32 v104, v104, v104
	v_fmac_f32_e32 v104, v101, v101
	v_and_b32_e32 v101, s100, v105
	v_fmac_f32_e32 v104, v101, v101
	v_lshlrev_b32_e32 v101, 16, v105
	v_fmac_f32_e32 v104, v101, v101
	v_and_b32_e32 v101, s100, v106
	v_fmac_f32_e32 v104, v101, v101
	v_lshlrev_b32_e32 v101, 16, v106
	v_fmac_f32_e32 v104, v101, v101
	v_and_b32_e32 v101, s100, v107
	v_fmac_f32_e32 v104, v101, v101
	v_lshlrev_b32_e32 v101, 16, v107
	v_fmac_f32_e32 v104, v101, v101
	s_waitcnt vmcnt(30)
	v_and_b32_e32 v101, s100, v108
	v_lshlrev_b32_e32 v108, 16, v108
	v_mul_f32_e32 v108, v108, v108
	v_fmac_f32_e32 v108, v101, v101
	v_and_b32_e32 v101, s100, v109
	v_fmac_f32_e32 v108, v101, v101
	v_lshlrev_b32_e32 v101, 16, v109
	v_fmac_f32_e32 v108, v101, v101
	v_and_b32_e32 v101, s100, v110
	v_fmac_f32_e32 v108, v101, v101
	v_lshlrev_b32_e32 v101, 16, v110
	v_fmac_f32_e32 v108, v101, v101
	v_and_b32_e32 v101, s100, v111
	v_fmac_f32_e32 v108, v101, v101
	v_lshlrev_b32_e32 v101, 16, v111
	v_fmac_f32_e32 v108, v101, v101
	s_waitcnt vmcnt(29)
	v_and_b32_e32 v101, s100, v112
	v_lshlrev_b32_e32 v112, 16, v112
	v_mul_f32_e32 v112, v112, v112
	v_fmac_f32_e32 v112, v101, v101
	v_and_b32_e32 v101, s100, v113
	v_fmac_f32_e32 v112, v101, v101
	v_lshlrev_b32_e32 v101, 16, v113
	v_fmac_f32_e32 v112, v101, v101
	v_and_b32_e32 v101, s100, v114
	v_fmac_f32_e32 v112, v101, v101
	v_lshlrev_b32_e32 v101, 16, v114
	v_fmac_f32_e32 v112, v101, v101
	v_and_b32_e32 v101, s100, v115
	v_fmac_f32_e32 v112, v101, v101
	v_lshlrev_b32_e32 v101, 16, v115
	v_fmac_f32_e32 v112, v101, v101
	s_waitcnt vmcnt(28)
	v_and_b32_e32 v101, s100, v116
	v_lshlrev_b32_e32 v116, 16, v116
	v_mul_f32_e32 v116, v116, v116
	v_fmac_f32_e32 v116, v101, v101
	v_and_b32_e32 v101, s100, v117
	v_fmac_f32_e32 v116, v101, v101
	v_lshlrev_b32_e32 v101, 16, v117
	v_fmac_f32_e32 v116, v101, v101
	v_and_b32_e32 v101, s100, v118
	v_fmac_f32_e32 v116, v101, v101
	v_lshlrev_b32_e32 v101, 16, v118
	v_fmac_f32_e32 v116, v101, v101
	v_and_b32_e32 v101, s100, v119
	v_fmac_f32_e32 v116, v101, v101
	v_lshlrev_b32_e32 v101, 16, v119
	v_fmac_f32_e32 v116, v101, v101
	v_add_f32_dpp v104, v104, v104 quad_perm:[1,0,3,2] row_mask:0xf bank_mask:0xf
	v_add_f32_dpp v108, v108, v108 quad_perm:[1,0,3,2] row_mask:0xf bank_mask:0xf
	v_add_f32_dpp v112, v112, v112 quad_perm:[1,0,3,2] row_mask:0xf bank_mask:0xf
	v_add_f32_dpp v116, v116, v116 quad_perm:[1,0,3,2] row_mask:0xf bank_mask:0xf
	v_add_f32_dpp v104, v104, v104 quad_perm:[2,3,0,1] row_mask:0xf bank_mask:0xf
	v_add_f32_dpp v108, v108, v108 quad_perm:[2,3,0,1] row_mask:0xf bank_mask:0xf
	v_add_f32_dpp v112, v112, v112 quad_perm:[2,3,0,1] row_mask:0xf bank_mask:0xf
	v_add_f32_dpp v116, v116, v116 quad_perm:[2,3,0,1] row_mask:0xf bank_mask:0xf
	v_add_f32_dpp v104, v104, v104 row_half_mirror row_mask:0xf bank_mask:0xf
	v_add_f32_dpp v108, v108, v108 row_half_mirror row_mask:0xf bank_mask:0xf
	v_add_f32_dpp v112, v112, v112 row_half_mirror row_mask:0xf bank_mask:0xf
	v_add_f32_dpp v116, v116, v116 row_half_mirror row_mask:0xf bank_mask:0xf
	v_max3_f32 v2, v2, v104, v108
	v_max3_f32 v2, v2, v112, v116
	s_waitcnt vmcnt(27)
	v_and_b32_e32 v101, s100, v120
	v_lshlrev_b32_e32 v120, 16, v120
	v_mul_f32_e32 v120, v120, v120
	v_fmac_f32_e32 v120, v101, v101
	v_and_b32_e32 v101, s100, v121
	v_fmac_f32_e32 v120, v101, v101
	v_lshlrev_b32_e32 v101, 16, v121
	v_fmac_f32_e32 v120, v101, v101
	v_and_b32_e32 v101, s100, v122
	v_fmac_f32_e32 v120, v101, v101
	v_lshlrev_b32_e32 v101, 16, v122
	v_fmac_f32_e32 v120, v101, v101
	v_and_b32_e32 v101, s100, v123
	v_fmac_f32_e32 v120, v101, v101
	v_lshlrev_b32_e32 v101, 16, v123
	v_fmac_f32_e32 v120, v101, v101
	s_waitcnt vmcnt(26)
	v_and_b32_e32 v101, s100, v124
	v_lshlrev_b32_e32 v124, 16, v124
	v_mul_f32_e32 v124, v124, v124
	v_fmac_f32_e32 v124, v101, v101
	v_and_b32_e32 v101, s100, v125
	v_fmac_f32_e32 v124, v101, v101
	v_lshlrev_b32_e32 v101, 16, v125
	v_fmac_f32_e32 v124, v101, v101
	v_and_b32_e32 v101, s100, v126
	v_fmac_f32_e32 v124, v101, v101
	v_lshlrev_b32_e32 v101, 16, v126
	v_fmac_f32_e32 v124, v101, v101
	v_and_b32_e32 v101, s100, v127
	v_fmac_f32_e32 v124, v101, v101
	v_lshlrev_b32_e32 v101, 16, v127
	v_fmac_f32_e32 v124, v101, v101
	s_waitcnt vmcnt(25)
	v_and_b32_e32 v101, s100, v128
	v_lshlrev_b32_e32 v128, 16, v128
	v_mul_f32_e32 v128, v128, v128
	v_fmac_f32_e32 v128, v101, v101
	v_and_b32_e32 v101, s100, v129
	v_fmac_f32_e32 v128, v101, v101
	v_lshlrev_b32_e32 v101, 16, v129
	v_fmac_f32_e32 v128, v101, v101
	v_and_b32_e32 v101, s100, v130
	v_fmac_f32_e32 v128, v101, v101
	v_lshlrev_b32_e32 v101, 16, v130
	v_fmac_f32_e32 v128, v101, v101
	v_and_b32_e32 v101, s100, v131
	v_fmac_f32_e32 v128, v101, v101
	v_lshlrev_b32_e32 v101, 16, v131
	v_fmac_f32_e32 v128, v101, v101
	s_waitcnt vmcnt(24)
	v_and_b32_e32 v101, s100, v132
	v_lshlrev_b32_e32 v132, 16, v132
	v_mul_f32_e32 v132, v132, v132
	v_fmac_f32_e32 v132, v101, v101
	v_and_b32_e32 v101, s100, v133
	v_fmac_f32_e32 v132, v101, v101
	v_lshlrev_b32_e32 v101, 16, v133
	v_fmac_f32_e32 v132, v101, v101
	v_and_b32_e32 v101, s100, v134
	v_fmac_f32_e32 v132, v101, v101
	v_lshlrev_b32_e32 v101, 16, v134
	v_fmac_f32_e32 v132, v101, v101
	v_and_b32_e32 v101, s100, v135
	v_fmac_f32_e32 v132, v101, v101
	v_lshlrev_b32_e32 v101, 16, v135
	v_fmac_f32_e32 v132, v101, v101
	v_add_f32_dpp v120, v120, v120 quad_perm:[1,0,3,2] row_mask:0xf bank_mask:0xf
	v_add_f32_dpp v124, v124, v124 quad_perm:[1,0,3,2] row_mask:0xf bank_mask:0xf
	v_add_f32_dpp v128, v128, v128 quad_perm:[1,0,3,2] row_mask:0xf bank_mask:0xf
	v_add_f32_dpp v132, v132, v132 quad_perm:[1,0,3,2] row_mask:0xf bank_mask:0xf
	v_add_f32_dpp v120, v120, v120 quad_perm:[2,3,0,1] row_mask:0xf bank_mask:0xf
	v_add_f32_dpp v124, v124, v124 quad_perm:[2,3,0,1] row_mask:0xf bank_mask:0xf
	v_add_f32_dpp v128, v128, v128 quad_perm:[2,3,0,1] row_mask:0xf bank_mask:0xf
	v_add_f32_dpp v132, v132, v132 quad_perm:[2,3,0,1] row_mask:0xf bank_mask:0xf
	v_add_f32_dpp v120, v120, v120 row_half_mirror row_mask:0xf bank_mask:0xf
	v_add_f32_dpp v124, v124, v124 row_half_mirror row_mask:0xf bank_mask:0xf
	v_add_f32_dpp v128, v128, v128 row_half_mirror row_mask:0xf bank_mask:0xf
	v_add_f32_dpp v132, v132, v132 row_half_mirror row_mask:0xf bank_mask:0xf
	v_max3_f32 v2, v2, v120, v124
	v_max3_f32 v2, v2, v128, v132
	s_waitcnt vmcnt(23)
	v_and_b32_e32 v101, s100, v136
	v_lshlrev_b32_e32 v136, 16, v136
	v_mul_f32_e32 v136, v136, v136
	v_fmac_f32_e32 v136, v101, v101
	v_and_b32_e32 v101, s100, v137
	v_fmac_f32_e32 v136, v101, v101
	v_lshlrev_b32_e32 v101, 16, v137
	v_fmac_f32_e32 v136, v101, v101
	v_and_b32_e32 v101, s100, v138
	v_fmac_f32_e32 v136, v101, v101
	v_lshlrev_b32_e32 v101, 16, v138
	v_fmac_f32_e32 v136, v101, v101
	v_and_b32_e32 v101, s100, v139
	v_fmac_f32_e32 v136, v101, v101
	v_lshlrev_b32_e32 v101, 16, v139
	v_fmac_f32_e32 v136, v101, v101
	s_waitcnt vmcnt(22)
	v_and_b32_e32 v101, s100, v140
	v_lshlrev_b32_e32 v140, 16, v140
	v_mul_f32_e32 v140, v140, v140
	v_fmac_f32_e32 v140, v101, v101
	v_and_b32_e32 v101, s100, v141
	v_fmac_f32_e32 v140, v101, v101
	v_lshlrev_b32_e32 v101, 16, v141
	v_fmac_f32_e32 v140, v101, v101
	v_and_b32_e32 v101, s100, v142
	v_fmac_f32_e32 v140, v101, v101
	v_lshlrev_b32_e32 v101, 16, v142
	v_fmac_f32_e32 v140, v101, v101
	v_and_b32_e32 v101, s100, v143
	v_fmac_f32_e32 v140, v101, v101
	v_lshlrev_b32_e32 v101, 16, v143
	v_fmac_f32_e32 v140, v101, v101
	s_waitcnt vmcnt(21)
	v_and_b32_e32 v101, s100, v144
	v_lshlrev_b32_e32 v144, 16, v144
	v_mul_f32_e32 v144, v144, v144
	v_fmac_f32_e32 v144, v101, v101
	v_and_b32_e32 v101, s100, v145
	v_fmac_f32_e32 v144, v101, v101
	v_lshlrev_b32_e32 v101, 16, v145
	v_fmac_f32_e32 v144, v101, v101
	v_and_b32_e32 v101, s100, v146
	v_fmac_f32_e32 v144, v101, v101
	v_lshlrev_b32_e32 v101, 16, v146
	v_fmac_f32_e32 v144, v101, v101
	v_and_b32_e32 v101, s100, v147
	v_fmac_f32_e32 v144, v101, v101
	v_lshlrev_b32_e32 v101, 16, v147
	v_fmac_f32_e32 v144, v101, v101
	s_waitcnt vmcnt(20)
	v_and_b32_e32 v101, s100, v148
	v_lshlrev_b32_e32 v148, 16, v148
	v_mul_f32_e32 v148, v148, v148
	v_fmac_f32_e32 v148, v101, v101
	v_and_b32_e32 v101, s100, v149
	v_fmac_f32_e32 v148, v101, v101
	v_lshlrev_b32_e32 v101, 16, v149
	v_fmac_f32_e32 v148, v101, v101
	v_and_b32_e32 v101, s100, v150
	v_fmac_f32_e32 v148, v101, v101
	v_lshlrev_b32_e32 v101, 16, v150
	v_fmac_f32_e32 v148, v101, v101
	v_and_b32_e32 v101, s100, v151
	v_fmac_f32_e32 v148, v101, v101
	v_lshlrev_b32_e32 v101, 16, v151
	v_fmac_f32_e32 v148, v101, v101
	v_add_f32_dpp v136, v136, v136 quad_perm:[1,0,3,2] row_mask:0xf bank_mask:0xf
	v_add_f32_dpp v140, v140, v140 quad_perm:[1,0,3,2] row_mask:0xf bank_mask:0xf
	v_add_f32_dpp v144, v144, v144 quad_perm:[1,0,3,2] row_mask:0xf bank_mask:0xf
	v_add_f32_dpp v148, v148, v148 quad_perm:[1,0,3,2] row_mask:0xf bank_mask:0xf
	v_add_f32_dpp v136, v136, v136 quad_perm:[2,3,0,1] row_mask:0xf bank_mask:0xf
	v_add_f32_dpp v140, v140, v140 quad_perm:[2,3,0,1] row_mask:0xf bank_mask:0xf
	v_add_f32_dpp v144, v144, v144 quad_perm:[2,3,0,1] row_mask:0xf bank_mask:0xf
	v_add_f32_dpp v148, v148, v148 quad_perm:[2,3,0,1] row_mask:0xf bank_mask:0xf
	v_add_f32_dpp v136, v136, v136 row_half_mirror row_mask:0xf bank_mask:0xf
	v_add_f32_dpp v140, v140, v140 row_half_mirror row_mask:0xf bank_mask:0xf
	v_add_f32_dpp v144, v144, v144 row_half_mirror row_mask:0xf bank_mask:0xf
	v_add_f32_dpp v148, v148, v148 row_half_mirror row_mask:0xf bank_mask:0xf
	v_max3_f32 v2, v2, v136, v140
	v_max3_f32 v2, v2, v144, v148
	s_waitcnt vmcnt(19)
	v_and_b32_e32 v101, s100, v152
	v_lshlrev_b32_e32 v152, 16, v152
	v_mul_f32_e32 v152, v152, v152
	v_fmac_f32_e32 v152, v101, v101
	v_and_b32_e32 v101, s100, v153
	v_fmac_f32_e32 v152, v101, v101
	v_lshlrev_b32_e32 v101, 16, v153
	v_fmac_f32_e32 v152, v101, v101
	v_and_b32_e32 v101, s100, v154
	v_fmac_f32_e32 v152, v101, v101
	v_lshlrev_b32_e32 v101, 16, v154
	v_fmac_f32_e32 v152, v101, v101
	v_and_b32_e32 v101, s100, v155
	v_fmac_f32_e32 v152, v101, v101
	v_lshlrev_b32_e32 v101, 16, v155
	v_fmac_f32_e32 v152, v101, v101
	s_waitcnt vmcnt(18)
	v_and_b32_e32 v101, s100, v156
	v_lshlrev_b32_e32 v156, 16, v156
	v_mul_f32_e32 v156, v156, v156
	v_fmac_f32_e32 v156, v101, v101
	v_and_b32_e32 v101, s100, v157
	v_fmac_f32_e32 v156, v101, v101
	v_lshlrev_b32_e32 v101, 16, v157
	v_fmac_f32_e32 v156, v101, v101
	v_and_b32_e32 v101, s100, v158
	v_fmac_f32_e32 v156, v101, v101
	v_lshlrev_b32_e32 v101, 16, v158
	v_fmac_f32_e32 v156, v101, v101
	v_and_b32_e32 v101, s100, v159
	v_fmac_f32_e32 v156, v101, v101
	v_lshlrev_b32_e32 v101, 16, v159
	v_fmac_f32_e32 v156, v101, v101
	s_waitcnt vmcnt(17)
	v_and_b32_e32 v101, s100, v160
	v_lshlrev_b32_e32 v160, 16, v160
	v_mul_f32_e32 v160, v160, v160
	v_fmac_f32_e32 v160, v101, v101
	v_and_b32_e32 v101, s100, v161
	v_fmac_f32_e32 v160, v101, v101
	v_lshlrev_b32_e32 v101, 16, v161
	v_fmac_f32_e32 v160, v101, v101
	v_and_b32_e32 v101, s100, v162
	v_fmac_f32_e32 v160, v101, v101
	v_lshlrev_b32_e32 v101, 16, v162
	v_fmac_f32_e32 v160, v101, v101
	v_and_b32_e32 v101, s100, v163
	v_fmac_f32_e32 v160, v101, v101
	v_lshlrev_b32_e32 v101, 16, v163
	v_fmac_f32_e32 v160, v101, v101
	s_waitcnt vmcnt(16)
	v_and_b32_e32 v101, s100, v164
	v_lshlrev_b32_e32 v164, 16, v164
	v_mul_f32_e32 v164, v164, v164
	v_fmac_f32_e32 v164, v101, v101
	v_and_b32_e32 v101, s100, v165
	v_fmac_f32_e32 v164, v101, v101
	v_lshlrev_b32_e32 v101, 16, v165
	v_fmac_f32_e32 v164, v101, v101
	v_and_b32_e32 v101, s100, v166
	v_fmac_f32_e32 v164, v101, v101
	v_lshlrev_b32_e32 v101, 16, v166
	v_fmac_f32_e32 v164, v101, v101
	v_and_b32_e32 v101, s100, v167
	v_fmac_f32_e32 v164, v101, v101
	v_lshlrev_b32_e32 v101, 16, v167
	v_fmac_f32_e32 v164, v101, v101
	v_add_f32_dpp v152, v152, v152 quad_perm:[1,0,3,2] row_mask:0xf bank_mask:0xf
	v_add_f32_dpp v156, v156, v156 quad_perm:[1,0,3,2] row_mask:0xf bank_mask:0xf
	v_add_f32_dpp v160, v160, v160 quad_perm:[1,0,3,2] row_mask:0xf bank_mask:0xf
	v_add_f32_dpp v164, v164, v164 quad_perm:[1,0,3,2] row_mask:0xf bank_mask:0xf
	v_add_f32_dpp v152, v152, v152 quad_perm:[2,3,0,1] row_mask:0xf bank_mask:0xf
	v_add_f32_dpp v156, v156, v156 quad_perm:[2,3,0,1] row_mask:0xf bank_mask:0xf
	v_add_f32_dpp v160, v160, v160 quad_perm:[2,3,0,1] row_mask:0xf bank_mask:0xf
	v_add_f32_dpp v164, v164, v164 quad_perm:[2,3,0,1] row_mask:0xf bank_mask:0xf
	v_add_f32_dpp v152, v152, v152 row_half_mirror row_mask:0xf bank_mask:0xf
	v_add_f32_dpp v156, v156, v156 row_half_mirror row_mask:0xf bank_mask:0xf
	v_add_f32_dpp v160, v160, v160 row_half_mirror row_mask:0xf bank_mask:0xf
	v_add_f32_dpp v164, v164, v164 row_half_mirror row_mask:0xf bank_mask:0xf
	v_max3_f32 v2, v2, v152, v156
	v_max3_f32 v2, v2, v160, v164
	s_waitcnt vmcnt(15)
	v_and_b32_e32 v101, s100, v168
	v_lshlrev_b32_e32 v168, 16, v168
	v_mul_f32_e32 v168, v168, v168
	v_fmac_f32_e32 v168, v101, v101
	v_and_b32_e32 v101, s100, v169
	v_fmac_f32_e32 v168, v101, v101
	v_lshlrev_b32_e32 v101, 16, v169
	v_fmac_f32_e32 v168, v101, v101
	v_and_b32_e32 v101, s100, v170
	v_fmac_f32_e32 v168, v101, v101
	v_lshlrev_b32_e32 v101, 16, v170
	v_fmac_f32_e32 v168, v101, v101
	v_and_b32_e32 v101, s100, v171
	v_fmac_f32_e32 v168, v101, v101
	v_lshlrev_b32_e32 v101, 16, v171
	v_fmac_f32_e32 v168, v101, v101
	s_waitcnt vmcnt(14)
	v_and_b32_e32 v101, s100, v172
	v_lshlrev_b32_e32 v172, 16, v172
	v_mul_f32_e32 v172, v172, v172
	v_fmac_f32_e32 v172, v101, v101
	v_and_b32_e32 v101, s100, v173
	v_fmac_f32_e32 v172, v101, v101
	v_lshlrev_b32_e32 v101, 16, v173
	v_fmac_f32_e32 v172, v101, v101
	v_and_b32_e32 v101, s100, v174
	v_fmac_f32_e32 v172, v101, v101
	v_lshlrev_b32_e32 v101, 16, v174
	v_fmac_f32_e32 v172, v101, v101
	v_and_b32_e32 v101, s100, v175
	v_fmac_f32_e32 v172, v101, v101
	v_lshlrev_b32_e32 v101, 16, v175
	v_fmac_f32_e32 v172, v101, v101
	s_waitcnt vmcnt(13)
	v_and_b32_e32 v101, s100, v176
	v_lshlrev_b32_e32 v176, 16, v176
	v_mul_f32_e32 v176, v176, v176
	v_fmac_f32_e32 v176, v101, v101
	v_and_b32_e32 v101, s100, v177
	v_fmac_f32_e32 v176, v101, v101
	v_lshlrev_b32_e32 v101, 16, v177
	v_fmac_f32_e32 v176, v101, v101
	v_and_b32_e32 v101, s100, v178
	v_fmac_f32_e32 v176, v101, v101
	v_lshlrev_b32_e32 v101, 16, v178
	v_fmac_f32_e32 v176, v101, v101
	v_and_b32_e32 v101, s100, v179
	v_fmac_f32_e32 v176, v101, v101
	v_lshlrev_b32_e32 v101, 16, v179
	v_fmac_f32_e32 v176, v101, v101
	s_waitcnt vmcnt(12)
	v_and_b32_e32 v101, s100, v180
	v_lshlrev_b32_e32 v180, 16, v180
	v_mul_f32_e32 v180, v180, v180
	v_fmac_f32_e32 v180, v101, v101
	v_and_b32_e32 v101, s100, v181
	v_fmac_f32_e32 v180, v101, v101
	v_lshlrev_b32_e32 v101, 16, v181
	v_fmac_f32_e32 v180, v101, v101
	v_and_b32_e32 v101, s100, v182
	v_fmac_f32_e32 v180, v101, v101
	v_lshlrev_b32_e32 v101, 16, v182
	v_fmac_f32_e32 v180, v101, v101
	v_and_b32_e32 v101, s100, v183
	v_fmac_f32_e32 v180, v101, v101
	v_lshlrev_b32_e32 v101, 16, v183
	v_fmac_f32_e32 v180, v101, v101
	v_add_f32_dpp v168, v168, v168 quad_perm:[1,0,3,2] row_mask:0xf bank_mask:0xf
	v_add_f32_dpp v172, v172, v172 quad_perm:[1,0,3,2] row_mask:0xf bank_mask:0xf
	v_add_f32_dpp v176, v176, v176 quad_perm:[1,0,3,2] row_mask:0xf bank_mask:0xf
	v_add_f32_dpp v180, v180, v180 quad_perm:[1,0,3,2] row_mask:0xf bank_mask:0xf
	v_add_f32_dpp v168, v168, v168 quad_perm:[2,3,0,1] row_mask:0xf bank_mask:0xf
	v_add_f32_dpp v172, v172, v172 quad_perm:[2,3,0,1] row_mask:0xf bank_mask:0xf
	v_add_f32_dpp v176, v176, v176 quad_perm:[2,3,0,1] row_mask:0xf bank_mask:0xf
	v_add_f32_dpp v180, v180, v180 quad_perm:[2,3,0,1] row_mask:0xf bank_mask:0xf
	v_add_f32_dpp v168, v168, v168 row_half_mirror row_mask:0xf bank_mask:0xf
	v_add_f32_dpp v172, v172, v172 row_half_mirror row_mask:0xf bank_mask:0xf
	v_add_f32_dpp v176, v176, v176 row_half_mirror row_mask:0xf bank_mask:0xf
	v_add_f32_dpp v180, v180, v180 row_half_mirror row_mask:0xf bank_mask:0xf
	v_max3_f32 v2, v2, v168, v172
	v_max3_f32 v2, v2, v176, v180
	s_waitcnt vmcnt(11)
	v_and_b32_e32 v101, s100, v184
	v_lshlrev_b32_e32 v184, 16, v184
	v_mul_f32_e32 v184, v184, v184
	v_fmac_f32_e32 v184, v101, v101
	v_and_b32_e32 v101, s100, v185
	v_fmac_f32_e32 v184, v101, v101
	v_lshlrev_b32_e32 v101, 16, v185
	v_fmac_f32_e32 v184, v101, v101
	v_and_b32_e32 v101, s100, v186
	v_fmac_f32_e32 v184, v101, v101
	v_lshlrev_b32_e32 v101, 16, v186
	v_fmac_f32_e32 v184, v101, v101
	v_and_b32_e32 v101, s100, v187
	v_fmac_f32_e32 v184, v101, v101
	v_lshlrev_b32_e32 v101, 16, v187
	v_fmac_f32_e32 v184, v101, v101
	s_waitcnt vmcnt(10)
	v_and_b32_e32 v101, s100, v188
	v_lshlrev_b32_e32 v188, 16, v188
	v_mul_f32_e32 v188, v188, v188
	v_fmac_f32_e32 v188, v101, v101
	v_and_b32_e32 v101, s100, v189
	v_fmac_f32_e32 v188, v101, v101
	v_lshlrev_b32_e32 v101, 16, v189
	v_fmac_f32_e32 v188, v101, v101
	v_and_b32_e32 v101, s100, v190
	v_fmac_f32_e32 v188, v101, v101
	v_lshlrev_b32_e32 v101, 16, v190
	v_fmac_f32_e32 v188, v101, v101
	v_and_b32_e32 v101, s100, v191
	v_fmac_f32_e32 v188, v101, v101
	v_lshlrev_b32_e32 v101, 16, v191
	v_fmac_f32_e32 v188, v101, v101
	s_waitcnt vmcnt(9)
	v_and_b32_e32 v101, s100, v192
	v_lshlrev_b32_e32 v192, 16, v192
	v_mul_f32_e32 v192, v192, v192
	v_fmac_f32_e32 v192, v101, v101
	v_and_b32_e32 v101, s100, v193
	v_fmac_f32_e32 v192, v101, v101
	v_lshlrev_b32_e32 v101, 16, v193
	v_fmac_f32_e32 v192, v101, v101
	v_and_b32_e32 v101, s100, v194
	v_fmac_f32_e32 v192, v101, v101
	v_lshlrev_b32_e32 v101, 16, v194
	v_fmac_f32_e32 v192, v101, v101
	v_and_b32_e32 v101, s100, v195
	v_fmac_f32_e32 v192, v101, v101
	v_lshlrev_b32_e32 v101, 16, v195
	v_fmac_f32_e32 v192, v101, v101
	s_waitcnt vmcnt(8)
	v_and_b32_e32 v101, s100, v196
	v_lshlrev_b32_e32 v196, 16, v196
	v_mul_f32_e32 v196, v196, v196
	v_fmac_f32_e32 v196, v101, v101
	v_and_b32_e32 v101, s100, v197
	v_fmac_f32_e32 v196, v101, v101
	v_lshlrev_b32_e32 v101, 16, v197
	v_fmac_f32_e32 v196, v101, v101
	v_and_b32_e32 v101, s100, v198
	v_fmac_f32_e32 v196, v101, v101
	v_lshlrev_b32_e32 v101, 16, v198
	v_fmac_f32_e32 v196, v101, v101
	v_and_b32_e32 v101, s100, v199
	v_fmac_f32_e32 v196, v101, v101
	v_lshlrev_b32_e32 v101, 16, v199
	v_fmac_f32_e32 v196, v101, v101
	v_add_f32_dpp v184, v184, v184 quad_perm:[1,0,3,2] row_mask:0xf bank_mask:0xf
	v_add_f32_dpp v188, v188, v188 quad_perm:[1,0,3,2] row_mask:0xf bank_mask:0xf
	v_add_f32_dpp v192, v192, v192 quad_perm:[1,0,3,2] row_mask:0xf bank_mask:0xf
	v_add_f32_dpp v196, v196, v196 quad_perm:[1,0,3,2] row_mask:0xf bank_mask:0xf
	v_add_f32_dpp v184, v184, v184 quad_perm:[2,3,0,1] row_mask:0xf bank_mask:0xf
	v_add_f32_dpp v188, v188, v188 quad_perm:[2,3,0,1] row_mask:0xf bank_mask:0xf
	v_add_f32_dpp v192, v192, v192 quad_perm:[2,3,0,1] row_mask:0xf bank_mask:0xf
	v_add_f32_dpp v196, v196, v196 quad_perm:[2,3,0,1] row_mask:0xf bank_mask:0xf
	v_add_f32_dpp v184, v184, v184 row_half_mirror row_mask:0xf bank_mask:0xf
	v_add_f32_dpp v188, v188, v188 row_half_mirror row_mask:0xf bank_mask:0xf
	v_add_f32_dpp v192, v192, v192 row_half_mirror row_mask:0xf bank_mask:0xf
	v_add_f32_dpp v196, v196, v196 row_half_mirror row_mask:0xf bank_mask:0xf
	v_max3_f32 v2, v2, v184, v188
	v_max3_f32 v2, v2, v192, v196
	s_waitcnt vmcnt(7)
	v_and_b32_e32 v101, s100, v200
	v_lshlrev_b32_e32 v200, 16, v200
	v_mul_f32_e32 v200, v200, v200
	v_fmac_f32_e32 v200, v101, v101
	v_and_b32_e32 v101, s100, v201
	v_fmac_f32_e32 v200, v101, v101
	v_lshlrev_b32_e32 v101, 16, v201
	v_fmac_f32_e32 v200, v101, v101
	v_and_b32_e32 v101, s100, v202
	v_fmac_f32_e32 v200, v101, v101
	v_lshlrev_b32_e32 v101, 16, v202
	v_fmac_f32_e32 v200, v101, v101
	v_and_b32_e32 v101, s100, v203
	v_fmac_f32_e32 v200, v101, v101
	v_lshlrev_b32_e32 v101, 16, v203
	v_fmac_f32_e32 v200, v101, v101
	s_waitcnt vmcnt(6)
	v_and_b32_e32 v101, s100, v204
	v_lshlrev_b32_e32 v204, 16, v204
	v_mul_f32_e32 v204, v204, v204
	v_fmac_f32_e32 v204, v101, v101
	v_and_b32_e32 v101, s100, v205
	v_fmac_f32_e32 v204, v101, v101
	v_lshlrev_b32_e32 v101, 16, v205
	v_fmac_f32_e32 v204, v101, v101
	v_and_b32_e32 v101, s100, v206
	v_fmac_f32_e32 v204, v101, v101
	v_lshlrev_b32_e32 v101, 16, v206
	v_fmac_f32_e32 v204, v101, v101
	v_and_b32_e32 v101, s100, v207
	v_fmac_f32_e32 v204, v101, v101
	v_lshlrev_b32_e32 v101, 16, v207
	v_fmac_f32_e32 v204, v101, v101
	s_waitcnt vmcnt(5)
	v_and_b32_e32 v101, s100, v208
	v_lshlrev_b32_e32 v208, 16, v208
	v_mul_f32_e32 v208, v208, v208
	v_fmac_f32_e32 v208, v101, v101
	v_and_b32_e32 v101, s100, v209
	v_fmac_f32_e32 v208, v101, v101
	v_lshlrev_b32_e32 v101, 16, v209
	v_fmac_f32_e32 v208, v101, v101
	v_and_b32_e32 v101, s100, v210
	v_fmac_f32_e32 v208, v101, v101
	v_lshlrev_b32_e32 v101, 16, v210
	v_fmac_f32_e32 v208, v101, v101
	v_and_b32_e32 v101, s100, v211
	v_fmac_f32_e32 v208, v101, v101
	v_lshlrev_b32_e32 v101, 16, v211
	v_fmac_f32_e32 v208, v101, v101
	s_waitcnt vmcnt(4)
	v_and_b32_e32 v101, s100, v212
	v_lshlrev_b32_e32 v212, 16, v212
	v_mul_f32_e32 v212, v212, v212
	v_fmac_f32_e32 v212, v101, v101
	v_and_b32_e32 v101, s100, v213
	v_fmac_f32_e32 v212, v101, v101
	v_lshlrev_b32_e32 v101, 16, v213
	v_fmac_f32_e32 v212, v101, v101
	v_and_b32_e32 v101, s100, v214
	v_fmac_f32_e32 v212, v101, v101
	v_lshlrev_b32_e32 v101, 16, v214
	v_fmac_f32_e32 v212, v101, v101
	v_and_b32_e32 v101, s100, v215
	v_fmac_f32_e32 v212, v101, v101
	v_lshlrev_b32_e32 v101, 16, v215
	v_fmac_f32_e32 v212, v101, v101
	v_add_f32_dpp v200, v200, v200 quad_perm:[1,0,3,2] row_mask:0xf bank_mask:0xf
	v_add_f32_dpp v204, v204, v204 quad_perm:[1,0,3,2] row_mask:0xf bank_mask:0xf
	v_add_f32_dpp v208, v208, v208 quad_perm:[1,0,3,2] row_mask:0xf bank_mask:0xf
	v_add_f32_dpp v212, v212, v212 quad_perm:[1,0,3,2] row_mask:0xf bank_mask:0xf
	v_add_f32_dpp v200, v200, v200 quad_perm:[2,3,0,1] row_mask:0xf bank_mask:0xf
	v_add_f32_dpp v204, v204, v204 quad_perm:[2,3,0,1] row_mask:0xf bank_mask:0xf
	v_add_f32_dpp v208, v208, v208 quad_perm:[2,3,0,1] row_mask:0xf bank_mask:0xf
	v_add_f32_dpp v212, v212, v212 quad_perm:[2,3,0,1] row_mask:0xf bank_mask:0xf
	v_add_f32_dpp v200, v200, v200 row_half_mirror row_mask:0xf bank_mask:0xf
	v_add_f32_dpp v204, v204, v204 row_half_mirror row_mask:0xf bank_mask:0xf
	v_add_f32_dpp v208, v208, v208 row_half_mirror row_mask:0xf bank_mask:0xf
	v_add_f32_dpp v212, v212, v212 row_half_mirror row_mask:0xf bank_mask:0xf
	v_max3_f32 v2, v2, v200, v204
	v_max3_f32 v2, v2, v208, v212
	s_waitcnt vmcnt(3)
	v_and_b32_e32 v101, s100, v216
	v_lshlrev_b32_e32 v216, 16, v216
	v_mul_f32_e32 v216, v216, v216
	v_fmac_f32_e32 v216, v101, v101
	v_and_b32_e32 v101, s100, v217
	v_fmac_f32_e32 v216, v101, v101
	v_lshlrev_b32_e32 v101, 16, v217
	v_fmac_f32_e32 v216, v101, v101
	v_and_b32_e32 v101, s100, v218
	v_fmac_f32_e32 v216, v101, v101
	v_lshlrev_b32_e32 v101, 16, v218
	v_fmac_f32_e32 v216, v101, v101
	v_and_b32_e32 v101, s100, v219
	v_fmac_f32_e32 v216, v101, v101
	v_lshlrev_b32_e32 v101, 16, v219
	v_fmac_f32_e32 v216, v101, v101
	s_waitcnt vmcnt(2)
	v_and_b32_e32 v101, s100, v220
	v_lshlrev_b32_e32 v220, 16, v220
	v_mul_f32_e32 v220, v220, v220
	v_fmac_f32_e32 v220, v101, v101
	v_and_b32_e32 v101, s100, v221
	v_fmac_f32_e32 v220, v101, v101
	v_lshlrev_b32_e32 v101, 16, v221
	v_fmac_f32_e32 v220, v101, v101
	v_and_b32_e32 v101, s100, v222
	v_fmac_f32_e32 v220, v101, v101
	v_lshlrev_b32_e32 v101, 16, v222
	v_fmac_f32_e32 v220, v101, v101
	v_and_b32_e32 v101, s100, v223
	v_fmac_f32_e32 v220, v101, v101
	v_lshlrev_b32_e32 v101, 16, v223
	v_fmac_f32_e32 v220, v101, v101
	s_waitcnt vmcnt(1)
	v_and_b32_e32 v101, s100, v224
	v_lshlrev_b32_e32 v224, 16, v224
	v_mul_f32_e32 v224, v224, v224
	v_fmac_f32_e32 v224, v101, v101
	v_and_b32_e32 v101, s100, v225
	v_fmac_f32_e32 v224, v101, v101
	v_lshlrev_b32_e32 v101, 16, v225
	v_fmac_f32_e32 v224, v101, v101
	v_and_b32_e32 v101, s100, v226
	v_fmac_f32_e32 v224, v101, v101
	v_lshlrev_b32_e32 v101, 16, v226
	v_fmac_f32_e32 v224, v101, v101
	v_and_b32_e32 v101, s100, v227
	v_fmac_f32_e32 v224, v101, v101
	v_lshlrev_b32_e32 v101, 16, v227
	v_fmac_f32_e32 v224, v101, v101
	s_waitcnt vmcnt(0)
	v_and_b32_e32 v101, s100, v228
	v_lshlrev_b32_e32 v228, 16, v228
	v_mul_f32_e32 v228, v228, v228
	v_fmac_f32_e32 v228, v101, v101
	v_and_b32_e32 v101, s100, v229
	v_fmac_f32_e32 v228, v101, v101
	v_lshlrev_b32_e32 v101, 16, v229
	v_fmac_f32_e32 v228, v101, v101
	v_and_b32_e32 v101, s100, v230
	v_fmac_f32_e32 v228, v101, v101
	v_lshlrev_b32_e32 v101, 16, v230
	v_fmac_f32_e32 v228, v101, v101
	v_and_b32_e32 v101, s100, v231
	v_fmac_f32_e32 v228, v101, v101
	v_lshlrev_b32_e32 v101, 16, v231
	v_fmac_f32_e32 v228, v101, v101
	v_add_f32_dpp v216, v216, v216 quad_perm:[1,0,3,2] row_mask:0xf bank_mask:0xf
	v_add_f32_dpp v220, v220, v220 quad_perm:[1,0,3,2] row_mask:0xf bank_mask:0xf
	v_add_f32_dpp v224, v224, v224 quad_perm:[1,0,3,2] row_mask:0xf bank_mask:0xf
	v_add_f32_dpp v228, v228, v228 quad_perm:[1,0,3,2] row_mask:0xf bank_mask:0xf
	v_add_f32_dpp v216, v216, v216 quad_perm:[2,3,0,1] row_mask:0xf bank_mask:0xf
	v_add_f32_dpp v220, v220, v220 quad_perm:[2,3,0,1] row_mask:0xf bank_mask:0xf
	v_add_f32_dpp v224, v224, v224 quad_perm:[2,3,0,1] row_mask:0xf bank_mask:0xf
	v_add_f32_dpp v228, v228, v228 quad_perm:[2,3,0,1] row_mask:0xf bank_mask:0xf
	v_add_f32_dpp v216, v216, v216 row_half_mirror row_mask:0xf bank_mask:0xf
	v_add_f32_dpp v220, v220, v220 row_half_mirror row_mask:0xf bank_mask:0xf
	v_add_f32_dpp v224, v224, v224 row_half_mirror row_mask:0xf bank_mask:0xf
	v_add_f32_dpp v228, v228, v228 row_half_mirror row_mask:0xf bank_mask:0xf
	v_max3_f32 v2, v2, v216, v220
	v_max3_f32 v2, v2, v224, v228
	v_mov_b32_e32 v3, v2
	v_mov_b32_e32 v4, v2
	v_max3_f32 v2, v2, v3, v4
	ds_bpermute_b32 v3, v20, v2
	s_waitcnt lgkmcnt(0)
	s_barrier
	v_max_f32_e32 v3, v3, v3
	v_max_f32_e32 v2, v2, v3
	ds_bpermute_b32 v3, v21, v2
	s_waitcnt lgkmcnt(0)
	v_max_f32_e32 v3, v3, v3
	v_max_f32_e32 v2, v2, v3
	ds_bpermute_b32 v3, v22, v2
	s_waitcnt lgkmcnt(0)
	v_max_f32_e32 v3, v3, v3
	v_max_f32_e32 v2, v2, v3
	ds_bpermute_b32 v3, v23, v2
	s_waitcnt lgkmcnt(0)
	v_max_f32_e32 v3, v3, v3
	v_max_f32_e32 v2, v2, v3
	ds_bpermute_b32 v3, v24, v2
	s_waitcnt lgkmcnt(0)
	v_max_f32_e32 v3, v3, v3
	v_max_f32_e32 v2, v2, v3
	ds_bpermute_b32 v3, v25, v2
	s_and_saveexec_b64 s[6:7], s[0:1]
	s_cbranch_execz .LBB0_389
	s_waitcnt lgkmcnt(0)
	v_max_f32_e32 v3, v3, v3
	v_max_f32_e32 v2, v2, v2
	v_max_f32_e32 v2, v2, v3
	v_mov_b32_e32 v3, s24
	ds_write_b32 v3, v2
